# v56 + layer-1 in-projection: the down-projection weight conversion runs only on the 192 workgroups with five tiles
# speedup vs baseline: 1.0070x; 1.0070x over previous
.LBB0_1989:
	s_and_b64 vcc, exec, s[0:1]
	s_cbranch_vccz .LBB0_2111
	v_readlane_b32 s0, v253, 45
	s_cmp_eq_u32 s0, 0
	s_cbranch_scc0 .LBB0_2111
	v_readlane_b32 s0, v253, 41
	v_readlane_b32 s1, v253, 42
	s_andn2_b64 vcc, exec, s[0:1]
	s_cbranch_vccnz .LBB0_1995
	s_abs_i32 s1, s30
	s_mul_hi_u32 s14, s1, s27
	s_mul_i32 s14, s14, s33
	s_sub_i32 s1, s1, s14
	s_ashr_i32 s0, s30, 31
	s_sub_i32 s14, s1, s33
	s_cmp_ge_u32 s1, s33
	s_cselect_b32 s1, s14, s1
	s_sub_i32 s14, s1, s33
	s_cmp_ge_u32 s1, s33
	s_cselect_b32 s1, s14, s1
	s_xor_b32 s1, s1, s0
	s_sub_i32 s0, s1, s0
	s_ashr_i32 s1, s0, 31
	s_and_b32 s1, s1, s72
	s_add_i32 s0, s1, s0
	s_lshr_b32 s1, s0, 3
	s_and_b32 s14, s1, 31
	s_cmp_lt_u32 s14, 8
	s_cbranch_scc1 .LBB0_1994
	s_lshr_b32 s1, s1, 5
	s_mul_i32 s1, s1, 24
	s_add_i32 s1, s1, s14
	s_add_i32 s1, s1, -8
	s_and_b32 s0, s0, 7
	s_lshl_b32 s1, s1, 3
	s_or_b32 s0, s0, s1
	s_cmpk_gt_i32 s0, 0x57f
	s_cbranch_scc1 .LBB0_1994
	v_readlane_b32 s14, v253, 32
	s_lshl_b32 s14, s14, 14
	s_lshl_b64 s[16:17], s[86:87], 3
	v_readlane_b32 s34, v250, 3
	v_readlane_b32 s35, v250, 4
	s_add_u32 s16, s34, s16
	s_addc_u32 s17, s35, s17
	s_load_dwordx2 s[16:17], s[16:17], 0x90
	v_readlane_b32 s15, v253, 33
	v_readlane_b32 s15, v253, 38
	s_mul_hi_u32 s1, s15, 0xb00000
	s_mul_i32 s15, s15, 0xb00000
	s_waitcnt lgkmcnt(0)
	s_add_u32 s15, s16, s15
	s_addc_u32 s17, s17, s1
	s_ashr_i32 s1, s0, 31
	s_lshr_b32 s1, s1, 27
	s_add_i32 s1, s0, s1
	s_ashr_i32 s1, s1, 5
	s_lshl_b32 s16, s1, 6
	s_lshl_b32 s1, s1, 10
	s_lshl_b32 s0, s0, 5
	s_sub_i32 s0, s0, s1
	s_ashr_i32 s1, s0, 31
	s_waitcnt vmcnt(0)
	v_lshrrev_b32_e32 v35, 3, v198
	s_lshl_b64 s[34:35], s[0:1], 2
	s_waitcnt vmcnt(0)
	v_or_b32_e32 v30, s16, v35
	s_add_u32 s34, s15, s34
	v_lshlrev_b32_e32 v0, 4, v198
	s_addc_u32 s35, s17, s35
	v_and_b32_e32 v0, 0x70, v0
	v_ashrrev_i32_e32 v31, 31, v30
	v_or_b32_e32 v6, 8, v30
	v_lshl_add_u64 v[32:33], s[34:35], 0, v[0:1]
	v_lshlrev_b64 v[2:3], 12, v[30:31]
	v_ashrrev_i32_e32 v7, 31, v6
	v_lshl_add_u64 v[2:3], v[32:33], 0, v[2:3]
	v_lshlrev_b64 v[6:7], 12, v[6:7]
	v_or_b32_e32 v10, 16, v30
	global_load_dwordx4 v[2:5], v[2:3], off
	v_lshl_add_u64 v[6:7], v[32:33], 0, v[6:7]
	v_ashrrev_i32_e32 v11, 31, v10
	global_load_dwordx4 v[6:9], v[6:7], off
	v_lshlrev_b64 v[10:11], 12, v[10:11]
	v_or_b32_e32 v14, 24, v30
	v_lshl_add_u64 v[10:11], v[32:33], 0, v[10:11]
	v_ashrrev_i32_e32 v15, 31, v14
	global_load_dwordx4 v[10:13], v[10:11], off
	v_lshlrev_b64 v[14:15], 12, v[14:15]
	v_or_b32_e32 v18, 32, v30
	v_lshl_add_u64 v[14:15], v[32:33], 0, v[14:15]
	v_ashrrev_i32_e32 v19, 31, v18
	global_load_dwordx4 v[14:17], v[14:15], off
	v_lshlrev_b64 v[18:19], 12, v[18:19]
	v_or_b32_e32 v22, 40, v30
	v_lshl_add_u64 v[18:19], v[32:33], 0, v[18:19]
	v_ashrrev_i32_e32 v23, 31, v22
	global_load_dwordx4 v[18:21], v[18:19], off
	v_lshlrev_b64 v[22:23], 12, v[22:23]
	v_or_b32_e32 v26, 48, v30
	v_lshl_add_u64 v[22:23], v[32:33], 0, v[22:23]
	v_ashrrev_i32_e32 v27, 31, v26
	global_load_dwordx4 v[22:25], v[22:23], off
	v_lshlrev_b64 v[26:27], 12, v[26:27]
	v_or_b32_e32 v30, 56, v30
	v_lshl_add_u64 v[26:27], v[32:33], 0, v[26:27]
	v_ashrrev_i32_e32 v31, 31, v30
	global_load_dwordx4 v[26:29], v[26:27], off
	v_lshlrev_b64 v[30:31], 12, v[30:31]
	v_lshl_add_u64 v[30:31], v[32:33], 0, v[30:31]
	global_load_dwordx4 v[30:33], v[30:31], off
	s_mul_hi_i32 s1, s0, 0x1600
	s_mulk_i32 s0, 0x1600
	s_add_u32 s15, s74, s0
	s_addc_u32 s29, s75, s1
	s_ashr_i32 s17, s16, 31
	v_and_b32_e32 v0, 7, v235
	s_lshl_b64 s[0:1], s[16:17], 1
	v_lshlrev_b32_e32 v34, 4, v0
	s_add_u32 s0, s15, s0
	v_or_b32_e32 v36, s14, v34
	s_movk_i32 s15, 0x84
	v_mad_u32_u24 v36, v35, s15, v36
	v_mul_u32_u24_e32 v0, 0x420, v0
	s_addc_u32 s1, s29, s1
	s_waitcnt vmcnt(7)
	ds_write2_b32 v36, v2, v3 offset1:1
	ds_write2_b32 v36, v4, v5 offset0:2 offset1:3
	v_add_u32_e32 v2, 0x420, v36
	s_waitcnt vmcnt(6)
	ds_write2_b32 v2, v6, v7 offset1:1
	v_add_u32_e32 v2, 0x428, v36
	ds_write2_b32 v2, v8, v9 offset1:1
	v_add_u32_e32 v2, 0x840, v36
	s_waitcnt vmcnt(5)
	ds_write2_b32 v2, v10, v11 offset1:1
	v_add_u32_e32 v2, 0x848, v36
	ds_write2_b32 v2, v12, v13 offset1:1
	v_add_u32_e32 v2, 0xc60, v36
	s_waitcnt vmcnt(4)
	ds_write2_b32 v2, v14, v15 offset1:1
	v_add_u32_e32 v2, 0xc68, v36
	ds_write2_b32 v2, v16, v17 offset1:1
	v_add_u32_e32 v2, 0x1080, v36
	s_waitcnt vmcnt(3)
	ds_write2_b32 v2, v18, v19 offset1:1
	v_add_u32_e32 v2, 0x1088, v36
	ds_write2_b32 v2, v20, v21 offset1:1
	v_add_u32_e32 v2, 0x14a0, v36
	s_waitcnt vmcnt(2)
	ds_write2_b32 v2, v22, v23 offset1:1
	v_add_u32_e32 v2, 0x14a8, v36
	ds_write2_b32 v2, v24, v25 offset1:1
	v_add_u32_e32 v2, 0x18c0, v36
	s_waitcnt vmcnt(1)
	ds_write2_b32 v2, v26, v27 offset1:1
	v_add_u32_e32 v2, 0x18c8, v36
	ds_write2_b32 v2, v28, v29 offset1:1
	v_add_u32_e32 v2, 0x1ce0, v36
	s_waitcnt vmcnt(0)
	ds_write2_b32 v2, v30, v31 offset1:1
	v_add_u32_e32 v2, 0x1ce8, v36
	ds_write2_b32 v2, v32, v33 offset1:1
	s_waitcnt lgkmcnt(0)
	v_lshlrev_b32_e32 v2, 2, v35
	v_or3_b32 v26, s14, v0, v2
	v_mul_u32_u24_e32 v0, 0xb00, v35
	ds_read2_b32 v[6:7], v26 offset0:33 offset1:41
	ds_read2_b32 v[8:9], v26 offset1:8
	ds_read2_b32 v[10:11], v26 offset0:66 offset1:74
	ds_read2_b32 v[12:13], v26 offset0:99 offset1:107
	ds_read2_b32 v[14:15], v26 offset0:132 offset1:140
	ds_read2_b32 v[16:17], v26 offset0:165 offset1:173
	ds_read2_b32 v[18:19], v26 offset0:198 offset1:206
	ds_read2_b32 v[20:21], v26 offset0:231 offset1:239
	v_lshlrev_b32_e32 v0, 1, v0
	v_lshl_add_u64 v[22:23], s[0:1], 0, v[0:1]
	v_mov_b32_e32 v35, v1
	v_lshl_add_u64 v[22:23], v[22:23], 0, v[34:35]
	s_mov_b32 s0, 0x1c00000
	v_add_co_u32_e32 v24, vcc, s0, v22
	s_mov_b32 s0, 0x1c0b000
	s_nop 0
	v_addc_co_u32_e32 v25, vcc, 0, v23, vcc
	s_waitcnt lgkmcnt(6)
	v_cvt_pk_bf16_f32 v2, v8, v6
	s_waitcnt lgkmcnt(4)
	v_cvt_pk_bf16_f32 v3, v10, v12
	s_waitcnt lgkmcnt(2)
	v_cvt_pk_bf16_f32 v4, v14, v16
	s_waitcnt lgkmcnt(0)
	v_cvt_pk_bf16_f32 v5, v18, v20
	v_add_co_u32_e32 v6, vcc, s0, v22
	global_store_dwordx4 v[24:25], v[2:5], off sc1
	s_mov_b32 s0, 0x1c16000
	s_nop 0
	v_cvt_pk_bf16_f32 v2, v9, v7
	v_cvt_pk_bf16_f32 v3, v11, v13
	v_cvt_pk_bf16_f32 v4, v15, v17
	v_cvt_pk_bf16_f32 v5, v19, v21
	v_addc_co_u32_e32 v7, vcc, 0, v23, vcc
	global_store_dwordx4 v[6:7], v[2:5], off sc1
	ds_read2_b32 v[6:7], v26 offset0:49 offset1:57
	ds_read2_b32 v[8:9], v26 offset0:16 offset1:24
	ds_read2_b32 v[10:11], v26 offset0:82 offset1:90
	ds_read2_b32 v[12:13], v26 offset0:115 offset1:123
	ds_read2_b32 v[14:15], v26 offset0:148 offset1:156
	ds_read2_b32 v[16:17], v26 offset0:181 offset1:189
	ds_read2_b32 v[18:19], v26 offset0:214 offset1:222
	ds_read2_b32 v[20:21], v26 offset0:247 offset1:255
	v_add_co_u32_e32 v24, vcc, s0, v22
	s_waitcnt lgkmcnt(6)
	v_cvt_pk_bf16_f32 v2, v8, v6
	v_addc_co_u32_e32 v25, vcc, 0, v23, vcc
	s_waitcnt lgkmcnt(4)
	v_cvt_pk_bf16_f32 v3, v10, v12
	s_waitcnt lgkmcnt(2)
	v_cvt_pk_bf16_f32 v4, v14, v16
	s_waitcnt lgkmcnt(0)
	v_cvt_pk_bf16_f32 v5, v18, v20
	v_add_co_u32_e32 v6, vcc, 0x1c21000, v22
	global_store_dwordx4 v[24:25], v[2:5], off sc1
	s_nop 1
	v_cvt_pk_bf16_f32 v2, v9, v7
	v_cvt_pk_bf16_f32 v3, v11, v13
	v_cvt_pk_bf16_f32 v4, v15, v17
	v_cvt_pk_bf16_f32 v5, v19, v21
	v_addc_co_u32_e32 v7, vcc, 0, v23, vcc
	global_store_dwordx4 v[6:7], v[2:5], off sc1
	s_waitcnt lgkmcnt(0)
